# GLA units of the mixer queues: the pop of the next unit (returning atomic by thread 0) moved from the unit top, where wave 0 waited for it ahead of the first barrier, to after the unit's first loads;
# baseline (speedup 1.0000x reference)
.LBB0_751:
	v_mov_b32_e32 v37, 0
	s_add_i32 s4, s52, 0xffffff00
	s_mul_hi_i32 s5, s4, 0x3e0f83e1
	s_lshr_b32 s6, s5, 31
	s_ashr_i32 s54, s5, 5
	s_add_i32 s54, s54, s6
	s_mul_i32 s5, s54, 0x84
	s_sub_i32 s52, s4, s5
	s_ashr_i32 s4, s54, 2
	s_cmp_gt_i32 s52, 3
	s_cselect_b64 s[20:21], -1, 0
	v_mov_b32 v39, v0
	s_mov_b64 s[6:7], -1
	v_readfirstlane_b32 s53, v39
	s_and_b64 vcc, exec, s[20:21]
	s_cbranch_vccz .LBB0_757
	s_ashr_i32 s5, s4, 31
	s_lshl_b64 s[6:7], s[4:5], 13
	s_lshl_b32 s5, s52, 6
	s_addk_i32 s5, 0xff00
	s_add_u32 s22, s6, s5
	s_addc_u32 s23, s7, 0
	s_mov_b64 s[6:7], 0

.Lglr_pre0:
	s_or_b64 exec, exec, s[24:25]
	s_mov_b64 s[98:99], exec
	s_and_b64 exec, exec, s[36:37]
	s_cbranch_execz .Ldq_skip_0
	v_mov_b32_e32 v37, 1
	global_atomic_add v37, v15, v37, s[10:11] sc0
.Ldq_skip_0:
	s_mov_b64 exec, s[98:99]
	s_barrier
	s_load_dwordx4 s[4:7], s[0:1], 0x88
	v_cmp_gt_i32_e32 vcc, s29, v39
	s_and_saveexec_b64 s[24:25], vcc
	s_cbranch_execz .LBB0_761
	s_waitcnt vmcnt(0)
	v_lshlrev_b32_e32 v24, 16, v20
	v_and_b32_e32 v25, 0xffff0000, v20
	v_lshlrev_b32_e32 v26, 16, v21
	v_and_b32_e32 v27, 0xffff0000, v21
	v_lshlrev_b32_e32 v20, 16, v22
	v_and_b32_e32 v21, 0xffff0000, v22
	v_lshlrev_b32_e32 v22, 16, v23
	v_and_b32_e32 v23, 0xffff0000, v23
	ds_write_b128 v14, v[24:27] offset:32768
	ds_write_b128 v14, v[20:23] offset:32784

.LBB0_1356:
	v_mov_b32_e32 v85, 0
	s_add_i32 s4, s85, 0xfffffce0
	s_mul_hi_i32 s5, s4, 0x3e0f83e1
	s_lshr_b32 s6, s5, 31
	s_ashr_i32 s67, s5, 5
	s_add_i32 s67, s67, s6
	s_mul_i32 s5, s67, 0x84
	s_sub_i32 s68, s4, s5
	s_ashr_i32 s4, s67, 2
	s_and_b32 s34, s67, 3
	s_cmp_lt_i32 s68, 4
	s_cselect_b64 s[6:7], -1, 0
	s_cmp_gt_i32 s68, 3
	s_cselect_b64 s[28:29], -1, 0
	s_ashr_i32 s5, s4, 31
	s_lshl_b32 s26, s4, 8
	s_lshl_b32 s14, s68, 6
	s_lshl_b64 s[24:25], s[4:5], 13
	s_ashr_i32 s27, s26, 31
	s_and_b64 s[4:5], s[6:7], exec
	s_cselect_b32 s4, s38, 0xffffff00
	s_cselect_b32 s5, s27, s25
	s_cselect_b32 s6, s26, s24
	s_add_i32 s4, s4, s14
	v_mov_b32 v87, v0
	s_add_u32 s26, s6, s4
	s_waitcnt vmcnt(3)
	v_ashrrev_i32_e32 v18, 3, v87
	s_addc_u32 s27, s5, 0
	v_ashrrev_i32_e32 v19, 31, v18
	s_waitcnt vmcnt(0)
	v_lshl_add_u64 v[2:3], s[26:27], 0, v[18:19]
	v_mad_u64_u32 v[4:5], s[4:5], v2, s39, v[76:77]
	v_and_b32_e32 v36, 7, v87
	v_mad_i32_i24 v5, v3, s39, v5
	s_lshl_b32 s14, s34, 7
	v_lshlrev_b32_e32 v74, 4, v36
	v_lshl_add_u64 v[2:3], v[4:5], 0, s[14:15]
	v_lshl_add_u64 v[2:3], v[2:3], 0, v[74:75]
	v_add_co_u32_e32 v2, vcc, s50, v2
	s_lshl_b32 s4, s34, 8
	s_nop 0
	v_addc_co_u32_e32 v3, vcc, 0, v3, vcc
	s_mov_b32 s5, s15
	global_load_dwordx4 v[14:17], v[2:3], off offset:512
	global_load_dwordx4 v[10:13], v[2:3], off offset:1024
	v_lshl_add_u64 v[2:3], v[4:5], 0, s[4:5]
	v_lshlrev_b32_e32 v74, 5, v36
	v_lshl_add_u64 v[2:3], v[2:3], 0, v[74:75]
	v_lshl_add_u64 v[4:5], v[2:3], 0, s[16:17]
	v_add_co_u32_e32 v2, vcc, 0x1000, v2
	v_readfirstlane_b32 s69, v87
	s_nop 0
	v_addc_co_u32_e32 v3, vcc, 0, v3, vcc
	global_load_dwordx4 v[6:9], v[2:3], off offset:1536
	s_nop 0
	global_load_dwordx4 v[2:5], v[4:5], off offset:16
	v_cmp_gt_i32_e32 vcc, s51, v87
	s_and_saveexec_b64 s[30:31], vcc
	s_cbranch_execz .Lglr_pre1
	v_ashrrev_i32_e32 v24, 2, v87
	v_ashrrev_i32_e32 v25, 31, v24
	v_lshl_add_u64 v[20:21], s[26:27], 0, v[24:25]
	v_mad_u64_u32 v[22:23], s[70:71], v20, s39, v[76:77]
	v_mov_b32_e32 v20, v23
	v_lshlrev_b32_e32 v19, 3, v87
	v_mad_u64_u32 v[20:21], s[70:71], v21, s39, v[20:21]
	v_and_b32_e32 v19, 24, v19
	v_mov_b32_e32 v23, v20
	v_lshlrev_b32_e32 v74, 1, v19
	v_lshl_add_u64 v[20:21], v[22:23], 0, v[74:75]
	v_add_co_u32_e32 v20, vcc, s50, v20
	v_lshlrev_b32_e32 v24, 7, v24
	s_nop 0
	v_addc_co_u32_e32 v21, vcc, 0, v21, vcc
	global_load_dwordx4 v[20:23], v[20:21], off offset:3584
	v_lshlrev_b32_e32 v19, 2, v19
	v_add3_u32 v19, 0, v24, v19
.Lglr_pre1:
	s_or_b64 exec, exec, s[30:31]
	s_load_dwordx4 s[4:7], s[0:1], 0x88
	s_load_dwordx2 s[24:25], s[0:1], 0x98
	v_cmp_gt_i32_e32 vcc, s51, v87
	s_waitcnt lgkmcnt(0)
	s_mov_b64 s[98:99], exec
	s_and_b64 exec, exec, s[36:37]
	s_cbranch_execz .Ldq_skip_1
	v_mov_b32_e32 v85, 1
	global_atomic_add v85, v75, v85, s[48:49] sc0
.Ldq_skip_1:
	s_mov_b64 exec, s[98:99]
	s_barrier
	s_and_saveexec_b64 s[30:31], vcc
	s_cbranch_execz .LBB0_1362
	s_waitcnt vmcnt(0)
	v_lshlrev_b32_e32 v24, 16, v20
	v_and_b32_e32 v25, 0xffff0000, v20
	v_lshlrev_b32_e32 v26, 16, v21
	v_and_b32_e32 v27, 0xffff0000, v21
	v_lshlrev_b32_e32 v20, 16, v22
	v_and_b32_e32 v21, 0xffff0000, v22
	v_lshlrev_b32_e32 v22, 16, v23
	v_and_b32_e32 v23, 0xffff0000, v23
	ds_write_b128 v19, v[24:27] offset:32768
	ds_write_b128 v19, v[20:23] offset:32784

.LBB0_2477:
	v_mov_b32_e32 v37, 0
	s_add_i32 s4, s66, 0xffffff00
	s_mul_hi_i32 s5, s4, 0x3e0f83e1
	s_lshr_b32 s6, s5, 31
	s_ashr_i32 s59, s5, 5
	s_add_i32 s59, s59, s6
	s_mul_i32 s5, s59, 0x84
	s_sub_i32 s57, s4, s5
	s_ashr_i32 s4, s59, 2
	s_cmp_gt_i32 s57, 3
	s_cselect_b64 s[22:23], -1, 0
	v_mov_b32 v39, v0
	s_mov_b64 s[6:7], -1
	v_readfirstlane_b32 s58, v39
	s_and_b64 vcc, exec, s[22:23]
	s_cbranch_vccz .LBB0_2483
	s_ashr_i32 s5, s4, 31
	s_lshl_b64 s[6:7], s[4:5], 13
	s_lshl_b32 s5, s57, 6
	s_addk_i32 s5, 0xff00
	s_add_u32 s24, s6, s5
	s_addc_u32 s25, s7, 0
	s_mov_b64 s[6:7], 0

.Lglr_pre2:
	s_or_b64 exec, exec, s[26:27]
	s_mov_b64 s[98:99], exec
	s_and_b64 exec, exec, s[36:37]
	s_cbranch_execz .Ldq_skip_2
	v_mov_b32_e32 v37, 1
	global_atomic_add v37, v15, v37, s[10:11] sc0
.Ldq_skip_2:
	s_mov_b64 exec, s[98:99]
	s_barrier
	s_load_dwordx4 s[4:7], s[0:1], 0x88
	v_cmp_gt_i32_e32 vcc, s31, v39
	s_and_saveexec_b64 s[26:27], vcc
	s_cbranch_execz .LBB0_2487
	s_waitcnt vmcnt(0)
	v_lshlrev_b32_e32 v24, 16, v20
	v_and_b32_e32 v25, 0xffff0000, v20
	v_lshlrev_b32_e32 v26, 16, v21
	v_and_b32_e32 v27, 0xffff0000, v21
	v_lshlrev_b32_e32 v20, 16, v22
	v_and_b32_e32 v21, 0xffff0000, v22
	v_lshlrev_b32_e32 v22, 16, v23
	v_and_b32_e32 v23, 0xffff0000, v23
	ds_write_b128 v14, v[24:27] offset:32768
	ds_write_b128 v14, v[20:23] offset:32784

.LBB0_2871:
	v_mov_b32_e32 v85, 0
	s_add_i32 s4, s85, 0xfffffd00
	s_ashr_i32 s5, s4, 31
	s_lshr_b32 s5, s5, 25
	s_add_i32 s5, s4, s5
	s_and_b32 s6, s5, 0xffffff80
	s_ashr_i32 s72, s5, 7
	s_sub_i32 s74, s4, s6
	s_add_i32 s73, s74, 4
	s_ashr_i32 s4, s5, 9
	s_and_b32 s38, s72, 3
	s_cmp_lt_i32 s74, 0
	s_cselect_b64 s[6:7], -1, 0
	s_cmp_gt_i32 s74, -1
	s_cselect_b64 s[30:31], -1, 0
	s_ashr_i32 s5, s4, 31
	s_lshl_b32 s28, s4, 8
	s_lshl_b32 s14, s73, 6
	s_lshl_b64 s[26:27], s[4:5], 13
	s_ashr_i32 s29, s28, 31
	s_and_b64 s[4:5], s[6:7], exec
	s_cselect_b32 s4, s50, 0xffffff00
	s_cselect_b32 s5, s29, s27
	s_cselect_b32 s6, s28, s26
	s_add_i32 s14, s14, s4
	v_mov_b32 v87, v0
	s_add_u32 s28, s6, s14
	v_ashrrev_i32_e32 v18, 3, v87
	s_addc_u32 s29, s5, 0
	v_ashrrev_i32_e32 v19, 31, v18
	v_lshl_add_u64 v[2:3], s[28:29], 0, v[18:19]
	v_mad_u64_u32 v[4:5], s[4:5], v2, s51, v[76:77]
	v_and_b32_e32 v36, 7, v87
	v_mad_i32_i24 v5, v3, s51, v5
	s_lshl_b32 s14, s38, 7
	v_lshlrev_b32_e32 v74, 4, v36
	v_lshl_add_u64 v[2:3], v[4:5], 0, s[14:15]
	v_lshl_add_u64 v[2:3], v[2:3], 0, v[74:75]
	v_add_co_u32_e32 v2, vcc, s52, v2
	s_lshl_b32 s4, s38, 8
	s_nop 0
	v_addc_co_u32_e32 v3, vcc, 0, v3, vcc
	s_mov_b32 s5, s15
	global_load_dwordx4 v[14:17], v[2:3], off offset:512
	global_load_dwordx4 v[10:13], v[2:3], off offset:1024
	v_lshl_add_u64 v[2:3], v[4:5], 0, s[4:5]
	v_lshlrev_b32_e32 v74, 5, v36
	v_lshl_add_u64 v[2:3], v[2:3], 0, v[74:75]
	v_lshl_add_u64 v[4:5], v[2:3], 0, s[16:17]
	v_add_co_u32_e32 v2, vcc, 0x1000, v2
	v_readfirstlane_b32 s75, v87
	s_nop 0
	v_addc_co_u32_e32 v3, vcc, 0, v3, vcc
	global_load_dwordx4 v[6:9], v[2:3], off offset:1536
	s_nop 0
	global_load_dwordx4 v[2:5], v[4:5], off offset:16
	v_cmp_gt_i32_e32 vcc, s53, v87
	s_and_saveexec_b64 s[34:35], vcc
	s_cbranch_execz .Lglr_pre3
	v_ashrrev_i32_e32 v24, 2, v87
	v_ashrrev_i32_e32 v25, 31, v24
	v_lshl_add_u64 v[20:21], s[28:29], 0, v[24:25]
	v_mad_u64_u32 v[22:23], s[76:77], v20, s51, v[76:77]
	v_mov_b32_e32 v20, v23
	v_lshlrev_b32_e32 v19, 3, v87
	v_mad_u64_u32 v[20:21], s[76:77], v21, s51, v[20:21]
	v_and_b32_e32 v19, 24, v19
	v_mov_b32_e32 v23, v20
	v_lshlrev_b32_e32 v74, 1, v19
	v_lshl_add_u64 v[20:21], v[22:23], 0, v[74:75]
	v_add_co_u32_e32 v20, vcc, s52, v20
	v_lshlrev_b32_e32 v24, 7, v24
	s_nop 0
	v_addc_co_u32_e32 v21, vcc, 0, v21, vcc
	global_load_dwordx4 v[20:23], v[20:21], off offset:3584
	v_lshlrev_b32_e32 v19, 2, v19
	v_add3_u32 v19, 0, v24, v19
.Lglr_pre3:
	s_or_b64 exec, exec, s[34:35]
	s_load_dwordx4 s[4:7], s[0:1], 0x88
	s_load_dwordx2 s[26:27], s[0:1], 0x98
	v_cmp_gt_i32_e32 vcc, s53, v87
	s_waitcnt lgkmcnt(0)
	s_mov_b64 s[98:99], exec
	s_and_b64 exec, exec, s[36:37]
	s_cbranch_execz .Ldq_skip_3
	v_mov_b32_e32 v85, 1
	global_atomic_add v85, v75, v85, s[48:49] sc0
.Ldq_skip_3:
	s_mov_b64 exec, s[98:99]
	s_barrier
	s_and_saveexec_b64 s[34:35], vcc
	s_cbranch_execz .LBB0_2877
	s_waitcnt vmcnt(0)
	v_lshlrev_b32_e32 v24, 16, v20
	v_and_b32_e32 v25, 0xffff0000, v20
	v_lshlrev_b32_e32 v26, 16, v21
	v_and_b32_e32 v27, 0xffff0000, v21
	v_lshlrev_b32_e32 v20, 16, v22
	v_and_b32_e32 v21, 0xffff0000, v22
	v_lshlrev_b32_e32 v22, 16, v23
	v_and_b32_e32 v23, 0xffff0000, v23
	ds_write_b128 v19, v[24:27] offset:32768
	ds_write_b128 v19, v[20:23] offset:32784
